# baseline (speedup 1.0000x reference)
_Z6gemm_qILi0ELi1EEvPKDF16_S1_iiiiiiPKfS3_S3_S3_PDF16_8ConvArgs:
	s_load_dwordx2 s[4:5], s[0:1], 0x10
	s_load_dwordx2 s[42:43], s[0:1], 0x40
	v_lshlrev_b32_e32 v103, 2, v0
	v_lshlrev_b32_e32 v1, 5, v0
	s_waitcnt lgkmcnt(0)
	s_ashr_i32 s3, s4, 31
	s_ashr_i32 s6, s5, 31
	s_lshr_b32 s3, s3, 24
	s_lshr_b32 s6, s6, 24
	s_add_i32 s3, s4, s3
	s_add_i32 s4, s5, s6
	s_ashr_i32 s3, s3, 8
	s_ashr_i32 s4, s4, 8
	s_mul_i32 s3, s4, s3
	s_mov_b64 s[4:5], -1
	s_cmp_lt_i32 s2, s3
	s_cbranch_scc0 .LBB6_3
	s_and_b64 vcc, exec, s[4:5]
	s_cbranch_vccnz .LBB6_26
